# as v43 plus GDN recurrence loop LDS operand reads issued as two ds_read_b64 instead of one ds_read2_b64 (LDS waits re-derived)
# baseline (speedup 1.0000x reference)
.LBB0_1555:
	s_add_i32 s18, s4, 2
	v_ashrrev_i32_e32 v107, 31, v106
	s_cmpk_lt_u32 s4, 0x7e
	v_lshlrev_b64 v[72:73], 11, v[106:107]
	s_waitcnt vmcnt(2)
	v_cvt_f32_f16_e32 v167, v160
	s_waitcnt vmcnt(1)
	v_cvt_f32_f16_e32 v168, v161
	s_cselect_b64 s[0:1], -1, 0
	v_lshl_add_u64 v[160:161], v[108:109], 0, v[72:73]
	s_and_b64 vcc, s[0:1], exec
	v_add_co_u32_e64 v192, s[0:1], s50, v160
	ds_read_b64 v[50:51], v142
	ds_read_b64 v[52:53], v142 offset:32
	ds_read_b64 v[30:31], v143
	ds_read_b64 v[32:33], v143 offset:32
	ds_read_b64 v[58:59], v142 offset:64
	ds_read_b64 v[60:61], v142 offset:96
	ds_read_b64 v[34:35], v143 offset:64
	ds_read_b64 v[36:37], v143 offset:96
	ds_read_b64 v[46:47], v142 offset:128
	ds_read_b64 v[48:49], v142 offset:160
	ds_read_b64 v[38:39], v143 offset:128
	ds_read_b64 v[40:41], v143 offset:160
	ds_read_b64 v[54:55], v142 offset:192
	ds_read_b64 v[56:57], v142 offset:224
	ds_read_b64 v[42:43], v143 offset:192
	ds_read_b64 v[44:45], v143 offset:224
	v_addc_co_u32_e64 v193, s[0:1], 0, v161, s[0:1]
	s_cselect_b32 s0, s18, 0x7f
	s_min_u32 s1, s4, 0x7c
	s_add_i32 s0, s0, s7
	s_add_i32 s1, s13, s1
	s_lshl_b32 s0, s0, 3
	s_waitcnt lgkmcnt(12)
	v_mfma_f32_16x16x32_f16 v[78:81], v[50:53], v[30:33], 0
	s_lshl_b32 s1, s1, 3
	s_or_b32 s0, s0, s6
	s_or_b32 s60, s1, s6
	s_waitcnt lgkmcnt(8)
	v_mfma_f32_16x16x32_f16 v[178:181], v[58:61], v[34:37], 0
	s_ashr_i32 s1, s0, 31
	s_ashr_i32 s61, s60, 31
	s_lshl_b64 s[64:65], s[0:1], 14
	s_lshl_b64 s[62:63], s[0:1], 13
	v_lshl_add_u64 v[82:83], s[0:1], 2, v[104:105]
	s_lshl_b64 s[0:1], s[60:61], 13
	v_lshl_add_u64 v[50:51], v[94:95], 0, s[64:65]
	s_waitcnt lgkmcnt(4)
	v_mfma_f32_16x16x32_f16 v[182:185], v[46:49], v[38:41], v[78:81]
	v_lshl_add_u64 v[202:203], v[92:93], 0, s[0:1]
	v_add_co_u32_e64 v188, s[0:1], s49, v50
	s_waitcnt lgkmcnt(0)
	v_mfma_f32_16x16x32_f16 v[54:57], v[54:57], v[42:45], v[178:181]
	v_mul_f32_e64 v64, v64, v70
	v_mul_f32_e64 v65, v65, v70
	v_pk_mul_f32 v[62:63], v[62:63], v[70:71] op_sel_hi:[1,0]
	v_pk_mul_f32 v[68:69], v[68:69], v[70:71] op_sel_hi:[1,0]
	v_pk_mul_f32 v[66:67], v[66:67], v[70:71] op_sel_hi:[1,0]
	v_add_u32_e32 v70, 64, v106
	v_lshl_add_u64 v[52:53], v[96:97], 0, s[64:65]
	v_addc_co_u32_e64 v189, s[0:1], 0, v51, s[0:1]
	v_ashrrev_i32_e32 v71, 31, v70
	v_add_co_u32_e64 v190, s[0:1], s49, v52
	v_lshlrev_b64 v[70:71], 11, v[70:71]
	v_lshl_add_u64 v[84:85], v[98:99], 0, s[64:65]
	v_addc_co_u32_e64 v191, s[0:1], 0, v53, s[0:1]
	v_pk_add_f32 v[56:57], v[184:185], v[56:57]
	v_pk_add_f32 v[54:55], v[182:183], v[54:55]
	v_lshl_add_u64 v[112:113], v[108:109], 0, v[70:71]
	global_load_dwordx4 v[58:61], v[50:51], off
	global_load_dwordx4 v[70:73], v[52:53], off
	global_load_dwordx4 v[74:77], v[84:85], off
	v_add_co_u32_e64 v84, s[0:1], s49, v84
	v_sub_f32_e32 v57, v157, v57
	v_sub_f32_e32 v56, v89, v56
	v_sub_f32_e32 v55, v88, v55
	v_sub_f32_e32 v54, v87, v54
	v_lshl_add_u64 v[174:175], v[92:93], 0, s[62:63]
	v_lshl_add_u64 v[176:177], v[110:111], 0, s[64:65]
	v_addc_co_u32_e64 v85, s[0:1], 0, v85, s[0:1]
	v_cvt_pk_f16_f32 v54, v54, v55
	v_cvt_pk_f16_f32 v55, v56, v57
	v_add_u32_e32 v115, 0x4000, v142
	global_load_dwordx4 v[50:53], v[174:175], off
	global_load_ushort v173, v[176:177], off
	s_nop 0
	global_load_ushort v174, v[176:177], off offset:256
	global_load_ushort v175, v[176:177], off offset:512
	s_nop 0
	global_load_ushort v176, v[176:177], off offset:768
	s_nop 0
	global_load_dword v107, v[82:83], off
	global_load_dwordx4 v[46:49], v[188:189], off
	global_load_dwordx4 v[78:81], v[190:191], off
	s_nop 0
	global_load_dwordx4 v[82:85], v[84:85], off
	ds_write_b64 v144, v[54:55]
	ds_read_b64 v[54:55], v115 offset:1024
	ds_read_b64 v[56:57], v115 offset:1056
	ds_read_b64 v[178:179], v115 offset:1088
	ds_read_b64 v[180:181], v115 offset:1120
	ds_read_b64 v[182:183], v115 offset:1152
	ds_read_b64 v[184:185], v115 offset:1184
	ds_read_b64 v[188:189], v115 offset:1216
	ds_read_b64 v[190:191], v115 offset:1248
	v_add_u32_e32 v164, 0xa800, v146
	s_waitcnt lgkmcnt(0)
	s_barrier
	s_waitcnt lgkmcnt(3)
	v_mfma_f32_16x16x32_f16 v[30:33], v[54:57], v[30:33], 0
	ds_read_b64 v[54:55], v164 offset:1024
	ds_read_b64 v[56:57], v164 offset:1056
	v_add_u32_e32 v163, 0x8800, v145
	v_add_u32_e32 v156, v140, v123
	s_waitcnt lgkmcnt(4)
	v_mfma_f32_16x16x32_f16 v[34:37], v[178:181], v[34:37], 0
	ds_read_b64 v[178:179], v147
	ds_read_b64 v[180:181], v147 offset:32
	v_add_u32_e32 v169, v90, v119
	v_add_u32_e32 v170, v141, v120
	s_waitcnt lgkmcnt(0)
	v_mfma_f32_16x16x32_f16 v[62:65], v[54:57], v[178:181], v[62:65]
	ds_read_b64 v[178:179], v148
	ds_read_b64 v[180:181], v148 offset:32
	v_add_u32_e32 v171, v90, v121
	v_add_u32_e32 v172, v141, v122
	v_mfma_f32_16x16x32_f16 v[30:33], v[182:185], v[38:41], v[30:33]
	ds_read_b64 v[38:39], v164 offset:1088
	ds_read_b64 v[40:41], v164 offset:1120
	s_lshl_b64 s[66:67], s[60:61], 14
	v_lshl_add_u64 v[196:197], v[94:95], 0, s[66:67]
	s_waitcnt lgkmcnt(2)
	v_mfma_f32_16x16x32_f16 v[54:57], v[54:57], v[178:181], v[66:69]
	v_cvt_f32_f16_e32 v165, v158
	v_add_u32_e32 v158, 0xf000, v142
	v_add_co_u32_e64 v206, s[0:1], s49, v196
	v_mfma_f32_16x16x32_f16 v[34:37], v[188:191], v[42:45], v[34:37]
	ds_read_b64 v[42:43], v147 offset:64
	ds_read_b64 v[44:45], v147 offset:96
	ds_read_b64 v[66:67], v163
	ds_read_b64 v[68:69], v163 offset:32
	v_lshl_add_u64 v[198:199], v[96:97], 0, s[66:67]
	v_addc_co_u32_e64 v207, s[0:1], 0, v197, s[0:1]
	s_waitcnt lgkmcnt(2)
	v_mfma_f32_16x16x32_f16 v[42:45], v[38:41], v[42:45], v[62:65]
	s_nop 2
	ds_read_b64 v[62:63], v148 offset:64
	ds_read_b64 v[64:65], v148 offset:96
	ds_read_b64 v[178:179], v156
	ds_read_b64 v[180:181], v156 offset:32
	v_add_co_u32_e64 v208, s[0:1], s49, v198
	s_waitcnt lgkmcnt(2)
	v_mfma_f32_16x16x32_f16 v[38:41], v[38:41], v[62:65], v[54:57]
	ds_read_b64 v[62:63], v156 offset:64
	ds_read_b64 v[64:65], v156 offset:96
	v_lshl_add_u64 v[200:201], v[98:99], 0, s[66:67]
	s_nop 0
	ds_read_b64 v[54:55], v163 offset:64
	ds_read_b64 v[56:57], v163 offset:96
	s_waitcnt lgkmcnt(4)
	v_mfma_f32_16x16x32_f16 v[30:33], v[66:69], v[178:181], v[30:33]
	v_addc_co_u32_e64 v209, s[0:1], 0, v199, s[0:1]
	v_add_co_u32_e64 v88, s[0:1], s49, v200
	s_waitcnt lgkmcnt(0)
	v_mfma_f32_16x16x32_f16 v[34:37], v[54:57], v[62:65], v[34:37]
	v_cvt_pk_f16_f32 v63, v44, v45
	v_cvt_pk_f16_f32 v62, v42, v43
	v_cvt_pk_f16_f32 v65, v40, v41
	v_cvt_pk_f16_f32 v64, v38, v39
	ds_write_b64 v149, v[62:63]
	ds_write_b64 v150, v[64:65]
	ds_write_b128 v135, v[2:5] offset:62464
	ds_write_b128 v169, v[6:9]
	ds_write_b128 v170, v[10:13]
	ds_write_b128 v137, v[14:17] offset:62464
	ds_write_b128 v171, v[18:21]
	ds_write_b128 v172, v[22:25]
	ds_write_b128 v151, v[26:29]
	v_add_f32_e32 v2, v30, v34
	v_add_f32_e32 v3, v31, v35
	v_cvt_f16_f32_e32 v2, v2
	v_add_f32_e32 v4, v32, v36
	v_cvt_f16_f32_e32 v3, v3
	v_add_f32_e32 v5, v33, v37
	v_cvt_f16_f32_e32 v4, v4
	v_cvt_f16_f32_e32 v5, v5
	global_store_short v[160:161], v2, off
	global_store_short v[160:161], v3, off offset:2048
	global_store_short v[192:193], v4, off
	global_store_short v[192:193], v5, off offset:2048
	s_waitcnt lgkmcnt(0)
	s_barrier
	global_load_dwordx4 v[2:5], v[196:197], off
	global_load_dwordx4 v[6:9], v[198:199], off
	ds_read_b64 v[26:27], v158 offset:1024
	ds_read_b64 v[28:29], v158 offset:1056
	v_addc_co_u32_e64 v89, s[0:1], 0, v201, s[0:1]
	global_load_dwordx4 v[10:13], v[200:201], off
	global_load_dwordx4 v[14:17], v[206:207], off
	ds_read_b64 v[62:63], v152
	ds_read_b64 v[64:65], v152 offset:32
	ds_read_b64 v[34:35], v158 offset:1088
	ds_read_b64 v[36:37], v158 offset:1120
	s_waitcnt vmcnt(20)
	v_pk_mul_f32 v[56:57], v[86:87], v[44:45] op_sel_hi:[0,1]
	v_pk_mul_f32 v[54:55], v[86:87], v[42:43] op_sel_hi:[0,1]
	v_pk_mul_f32 v[180:181], v[86:87], v[40:41] op_sel_hi:[0,1]
	v_pk_mul_f32 v[178:179], v[86:87], v[38:39] op_sel_hi:[0,1]
	global_load_dwordx4 v[18:21], v[208:209], off
	global_load_dwordx4 v[22:25], v[88:89], off
	ds_read_b64 v[86:87], v152 offset:64
	ds_read_b64 v[88:89], v152 offset:96
	ds_read_b64 v[38:39], v158 offset:1152
	ds_read_b64 v[40:41], v158 offset:1184
	v_lshl_add_u64 v[204:205], v[110:111], 0, s[66:67]
	v_cvt_f32_f16_e32 v166, v159
	v_lshl_add_u64 v[194:195], s[60:61], 2, v[104:105]
	s_waitcnt lgkmcnt(6)
	v_mfma_f32_16x16x32_f16 v[42:45], v[26:29], v[62:65], 0
	global_load_dwordx4 v[26:29], v[202:203], off
	ds_read_b64 v[30:31], v152 offset:128
	ds_read_b64 v[32:33], v152 offset:160
	ds_read_b64 v[66:67], v158 offset:1216
	ds_read_b64 v[68:69], v158 offset:1248
	global_load_ushort v158, v[204:205], off
	global_load_ushort v159, v[204:205], off offset:256
	s_waitcnt lgkmcnt(6)
	v_mfma_f32_16x16x32_f16 v[182:185], v[34:37], v[86:89], 0
	ds_read_b64 v[34:35], v152 offset:192
	ds_read_b64 v[36:37], v152 offset:224
	global_load_ushort v160, v[204:205], off offset:512
	global_load_ushort v161, v[204:205], off offset:768
	global_load_dword v163, v[194:195], off
	v_add_co_u32_e64 v114, s[4:5], s50, v112
	s_waitcnt lgkmcnt(4)
	v_mfma_f32_16x16x32_f16 v[38:41], v[38:41], v[30:33], v[42:45]
	v_addc_co_u32_e64 v115, s[0:1], 0, v113, s[4:5]
	s_waitcnt vmcnt(20)
	v_cvt_f32_f16_e32 v157, v176
	s_waitcnt lgkmcnt(0)
	v_mfma_f32_16x16x32_f16 v[42:45], v[66:69], v[34:37], v[182:185]
	v_add_u32_e32 v106, 0x80, v106
	s_mov_b32 s4, s18
	s_nop 5
	v_add_f32_e32 v38, v38, v42
	v_add_f32_e32 v39, v39, v43
	v_add_f32_e32 v40, v40, v44
	v_add_f32_e32 v41, v41, v45
	v_sub_f32_e32 v38, v165, v38
	v_sub_f32_e32 v42, v166, v39
	v_sub_f32_e32 v39, v167, v40
	v_sub_f32_e32 v40, v168, v41
	v_cvt_pk_f16_f32 v39, v39, v40
	v_cvt_pk_f16_f32 v38, v38, v42
	ds_write_b64 v144, v[38:39]
	ds_read_b64 v[66:67], v153
	ds_read_b64 v[68:69], v153 offset:32
	ds_read_b64 v[164:165], v153 offset:64
	ds_read_b64 v[166:167], v153 offset:96
	ds_read_b64 v[42:43], v153 offset:128
	ds_read_b64 v[44:45], v153 offset:160
	ds_read_b64 v[38:39], v153 offset:192
	ds_read_b64 v[40:41], v153 offset:224
	s_waitcnt lgkmcnt(0)
	s_barrier
	ds_read_b64 v[168:169], v155
	ds_read_b64 v[170:171], v155 offset:32
	s_waitcnt lgkmcnt(5)
	v_mfma_f32_16x16x32_f16 v[66:69], v[66:69], v[62:65], 0
	ds_read_b64 v[62:63], v147
	ds_read_b64 v[64:65], v147 offset:32
	s_waitcnt lgkmcnt(5)
	v_mfma_f32_16x16x32_f16 v[30:33], v[42:45], v[30:33], v[66:69]
	ds_read_b64 v[42:43], v155 offset:64
	ds_read_b64 v[44:45], v155 offset:96
	v_mfma_f32_16x16x32_f16 v[86:89], v[164:167], v[86:89], 0
	s_waitcnt lgkmcnt(2)
	v_mfma_f32_16x16x32_f16 v[62:65], v[168:171], v[62:65], v[54:57]
	s_nop 2
	ds_read_b64 v[54:55], v148
	ds_read_b64 v[56:57], v148 offset:32
	v_mfma_f32_16x16x32_f16 v[34:37], v[38:41], v[34:37], v[86:89]
	ds_read_b64 v[38:39], v147 offset:64
	ds_read_b64 v[40:41], v147 offset:96
	s_nop 1
	ds_read_b64 v[86:87], v154
	ds_read_b64 v[88:89], v154 offset:32
	s_waitcnt lgkmcnt(4)
	v_mfma_f32_16x16x32_f16 v[54:57], v[168:171], v[54:57], v[178:181]
	s_waitcnt lgkmcnt(2)
	v_mfma_f32_16x16x32_f16 v[62:65], v[42:45], v[38:41], v[62:65]
	ds_read_b64 v[38:39], v148 offset:64
	ds_read_b64 v[40:41], v148 offset:96
	ds_read_b64 v[164:165], v156
	ds_read_b64 v[166:167], v156 offset:32
	s_waitcnt lgkmcnt(2)
	v_mfma_f32_16x16x32_f16 v[66:69], v[42:45], v[38:41], v[54:57]
	ds_read_b64 v[38:39], v154 offset:64
	ds_read_b64 v[40:41], v154 offset:96
	ds_read_b64 v[42:43], v156 offset:64
	ds_read_b64 v[44:45], v156 offset:96
	s_waitcnt lgkmcnt(4)
	v_mfma_f32_16x16x32_f16 v[30:33], v[86:89], v[164:167], v[30:33]
	v_cvt_f32_f16_e32 v87, v173
	v_cvt_f32_f16_e32 v88, v174
	v_cvt_f32_f16_e32 v89, v175
	s_waitcnt lgkmcnt(0)
	v_mfma_f32_16x16x32_f16 v[34:37], v[38:41], v[42:45], v[34:37]
	v_cvt_pk_f16_f32 v39, v64, v65
	v_cvt_pk_f16_f32 v38, v62, v63
	v_cvt_pk_f16_f32 v41, v68, v69
	s_nop 4
	v_add_f32_e32 v30, v30, v34
	v_add_f32_e32 v31, v31, v35
	v_cvt_f16_f32_e32 v30, v30
	v_add_f32_e32 v32, v32, v36
	v_cvt_f16_f32_e32 v31, v31
	v_add_f32_e32 v33, v33, v37
	v_cvt_f16_f32_e32 v32, v32
	v_cvt_f16_f32_e32 v33, v33
	v_cvt_pk_f16_f32 v40, v66, v67
	ds_write_b64 v133, v[38:39]
	ds_write_b64 v134, v[40:41]
	ds_write_b128 v135, v[58:61]
	ds_write_b128 v135, v[70:73] offset:17408
	ds_write_b128 v136, v[74:77] offset:44032
	s_waitcnt vmcnt(18)
	ds_write_b128 v137, v[46:49]
	s_waitcnt vmcnt(17)
	ds_write_b128 v137, v[78:81] offset:17408
	s_waitcnt vmcnt(16)
	ds_write_b128 v138, v[82:85] offset:44032
	ds_write_b128 v139, v[50:53] offset:34816
	global_store_short v[112:113], v30, off
	global_store_short v[112:113], v31, off offset:2048
	global_store_short v[114:115], v32, off
	global_store_short v[114:115], v33, off offset:2048
	s_waitcnt lgkmcnt(0)
	s_barrier
	v_mov_b32_e32 v70, v107
	s_waitcnt vmcnt(4)
	v_mov_b32_e32 v86, v163
	s_cbranch_vccnz .LBB0_1555
	s_waitcnt lgkmcnt(0)
	s_barrier
	s_branch .LBB0_1544
